# gather: one static s_setprio 1 for waves 4-7 (younger half) for the whole token loop, reset at phase exit
# speedup vs baseline: 1.0105x; 1.0021x over previous
; __device__ __forceinline__ int fresh_lane() { unsigned z = 0u; asm volatile("" : "+v"(z)); return (int)__builtin_amdgcn_mbcnt_hi(~0u, __builtin_amdgcn_mbcnt_lo(~0u, z)); }
; #define GATHER_ISSUE(k, sn_) do { const int sn = (sn_); const int secn = (sn >> 6) & 3; \
;         const int idsel = (sn >= 256) ? id0n : ((secn & 1) ? id1 : id0); \
;         const unsigned so = (unsigned)__builtin_amdgcn_readlane(idsel, sn & 63) * ROW4 + ((secn >= 2) ? TAB4 : 0u); \
;         ring[k] = __builtin_bit_cast(v4u, __builtin_amdgcn_raw_buffer_load_b128(rs, voff, so, 0)); } while (0)
;     const unsigned char* UV4 = (const unsigned char*)(F.ws + WS_UB) + (size_t)layer * (2u * TAB4);
;     const bf16* ZB = (const bf16*)(F.ws + WS_ZF); const bf16* PLE = (const bf16*)(F.ws + WS_PLE);
;     const int* IDX = (const int*)(F.ws + WS_IDX); const float* GWt = (const float*)(F.ws + WS_GW);
;     float* OF = (layer == 3 && !dummy) ? F.out : (float*)nullptr; bf16* XB = (bf16*)(F.ws + (dummy ? WS_X1B : WS_XB));
;     ...
;     const int idmask = (dummy == 1) ? PROBE_GATHER_MASK : 0x3fff;
;     ...
;     const float* gain1 = F.ln_gain + (size_t)(layer * 2) * D; const float* bias1 = F.ln_bias + (size_t)(layer * 2) * D;
;     const float* gain = F.ln_gain + (size_t)(layer * 2 + 1) * D; const float* bias = F.ln_bias + (size_t)(layer * 2 + 1) * D;
;     const int lane = fresh_lane();
;     const bool b3 = (lane & 8) != 0, b2 = (lane & 4) != 0, b1 = (lane & 2) != 0, b0 = (lane & 1) != 0;
;     const __amdgpu_buffer_rsrc_t rs = __builtin_amdgcn_make_buffer_rsrc((void*)UV4, (short)0, (int)(2u * TAB4), 0x00020000);
;     const unsigned voff = (unsigned)lane * 16u;
;     v4u ring[16];
;     int id0 = 0, id1 = 0, id0n = 0;
;     ...
;     int id1n = 0; float g0n = 0.f, g1n = 0.f;
;     if (F.gw < T) { gather_sorted_ids(IDX, GWt, F.gw, lane, id0n, id1n, g0n, g1n);
;     ...
;         id0n &= idmask; id1n &= idmask;
;     ...
; #pragma unroll
;         for (int k = 0; k < 16; ++k) GATHER_ISSUE(k, 256 + k); }
.LBB0_1412:
	s_andn2_b64 vcc, exec, s[14:15]
	s_cbranch_vccnz .LBB0_1452
	s_add_u32 s8, s60, 0x4a600000
	v_writelane_b32 v254, s8, 56
	s_addc_u32 s8, s61, 0
	v_writelane_b32 v255, s8, 5
	s_add_u32 s8, s60, 0x66600000
	v_writelane_b32 v255, s8, 7
	s_addc_u32 s8, s61, 0
	s_cmp_eq_u32 s18, 3
	v_writelane_b32 v255, s8, 9
	s_cselect_b64 s[8:9], -1, 0
	s_add_u32 s10, s60, 0x36600000
	v_writelane_b32 v255, s10, 11
	s_addc_u32 s43, s61, 0
	s_lshl_b32 s10, s18, 1
	s_mov_b64 s[16:17], s[80:81]
	v_writelane_b32 v255, s76, 1
	s_mov_b64 s[18:19], s[82:83]
	s_mov_b64 s[20:21], s[84:85]
	s_mov_b64 s[22:23], s[86:87]
	v_writelane_b32 v255, s77, 2
	v_readlane_b32 s76, v254, 1
	s_ashr_i32 s11, s10, 31
	v_readlane_b32 s90, v254, 15
	v_readlane_b32 s91, v254, 16
	s_lshl_b64 s[12:13], s[10:11], 13
	s_mov_b64 s[14:15], s[90:91]
	s_add_u32 s36, s14, s12
	s_addc_u32 s37, s15, s13
	s_add_u32 s12, s16, s12
	s_addc_u32 s13, s17, s13
	s_or_b32 s10, s10, 1
	v_readlane_b32 s72, v255, 1
	s_ashr_i32 s11, s10, 31
	v_readlane_b32 s73, v255, 2
	v_writelane_b32 v255, s12, 13
	s_lshl_b64 s[10:11], s[10:11], 13
	v_readlane_b32 s80, v254, 5
	v_writelane_b32 v255, s13, 14
	s_add_u32 s12, s14, s10
	s_addc_u32 s13, s15, s11
	v_readlane_b32 s81, v254, 6
	s_add_u32 s80, s16, s10
	s_addc_u32 s81, s17, s11
	v_readlane_b32 s10, v254, 51
	v_readlane_b32 s82, v254, 7
	v_readlane_b32 s83, v254, 8
	v_readlane_b32 s11, v254, 52
	s_and_b64 s[82:83], s[8:9], s[10:11]
	s_add_u32 s30, s60, 0x57600000
	v_writelane_b32 v255, s12, 15
	s_addc_u32 s39, s61, 0
	s_add_u32 s8, s60, 0x53200000
	v_writelane_b32 v255, s13, 16
	v_writelane_b32 v255, s8, 33
	s_addc_u32 s8, s61, 0
	v_writelane_b32 v255, s8, 35
	s_add_u32 s8, s60, 0x53600000
	v_writelane_b32 v255, s8, 29
	s_addc_u32 s8, s61, 0
	v_cmp_eq_u32_e64 s[28:29], 0, v68
	v_cmp_eq_u32_e32 vcc, 0, v67
	v_writelane_b32 v255, s8, 31
	s_xor_b64 s[44:45], vcc, s[28:29]
	v_cmp_eq_u32_e64 s[20:21], 0, v69
	v_writelane_b32 v255, s44, 17
	v_lshlrev_b32_e32 v70, 5, v130
	v_ashrrev_i32_e32 v71, 31, v70
	v_writelane_b32 v255, s45, 18
	s_xor_b64 s[44:45], vcc, s[20:21]
	v_writelane_b32 v255, s44, 19
	v_add_u32_e32 v194, 4, v66
	v_add_u32_e32 v195, 8, v66
	v_writelane_b32 v255, s45, 20
	s_xor_b64 s[44:45], vcc, s[0:1]
	v_writelane_b32 v255, s44, 21
	v_add_u32_e32 v196, 12, v66
	v_lshl_add_u64 v[66:67], s[60:61], 0, v[70:71]
	v_writelane_b32 v255, s45, 22
	s_xor_b64 s[44:45], vcc, s[2:3]
	v_writelane_b32 v255, s44, 23
	s_xor_b64 s[8:9], s[4:5], s[6:7]
	s_xor_b64 s[10:11], s[2:3], s[4:5]
	v_writelane_b32 v255, s45, 24
	s_xor_b64 s[44:45], vcc, s[4:5]
	v_writelane_b32 v255, s44, 25
	s_xor_b64 s[12:13], s[2:3], s[6:7]
	s_xor_b64 s[14:15], s[0:1], s[2:3]
	v_writelane_b32 v255, s45, 26
	s_xor_b64 s[44:45], vcc, s[6:7]
	v_writelane_b32 v255, s44, 27
	s_xor_b64 s[16:17], s[0:1], s[4:5]
	s_xor_b64 s[18:19], s[0:1], s[6:7]
	v_writelane_b32 v255, s45, 28
	s_mov_b64 s[44:45], 0x55600000
	s_xor_b64 s[22:23], s[20:21], s[0:1]
	s_xor_b64 s[24:25], s[20:21], s[2:3]
	s_xor_b64 s[26:27], s[20:21], s[4:5]
	v_ashrrev_i32_e32 v193, 4, v130
	v_lshl_add_u64 v[132:133], v[66:67], 0, s[44:45]
	s_xor_b64 s[44:45], s[20:21], s[6:7]
	s_xor_b64 s[46:47], s[28:29], s[20:21]
	s_xor_b64 s[48:49], s[28:29], s[0:1]
	s_xor_b64 s[50:51], s[28:29], s[2:3]
	s_xor_b64 s[52:53], s[28:29], s[4:5]
	s_xor_b64 s[54:55], s[28:29], s[6:7]
	v_readlane_b32 s77, v254, 2
	v_readlane_b32 s78, v254, 3
	v_readlane_b32 s79, v254, 4
	v_readlane_b32 s84, v254, 9
	v_readlane_b32 s85, v254, 10
	v_readlane_b32 s86, v254, 11
	v_readlane_b32 s87, v254, 12
	v_readlane_b32 s88, v254, 13
	v_readlane_b32 s89, v254, 14
	v_readlane_b32 s98, v254, 55
	s_lshl_b32 s98, s98, 6
	v_add_u32_e32 v228, s98, v130
	v_lshlrev_b32_e32 v228, 4, v228
	global_load_dwordx4 v[212:215], v228, s[36:37]
	global_load_dwordx4 v[224:227], v228, s[80:81]
	v_readlane_b32 s98, v255, 13
	v_readlane_b32 s99, v255, 14
	s_nop 4
	global_load_dwordx4 v[216:219], v228, s[98:99]
	v_readlane_b32 s98, v255, 15
	v_readlane_b32 s99, v255, 16
	s_nop 4
	global_load_dwordx4 v[220:223], v228, s[98:99]
	s_waitcnt vmcnt(3)
	ds_write_b128 v228, v[212:215]
	s_waitcnt vmcnt(2)
	ds_write_b128 v228, v[224:227] offset:24576
	s_waitcnt vmcnt(1)
	ds_write_b128 v228, v[216:219] offset:8192
	s_waitcnt vmcnt(0)
	ds_write_b128 v228, v[220:223] offset:16384
	s_waitcnt lgkmcnt(0)
	s_barrier
	v_readlane_b32 s100, v254, 58
	v_readlane_b32 s99, v255, 1
	s_add_i32 s99, s100, s99
	s_cmp_lt_i32 s99, 0x4000
	s_cselect_b32 s99, s99, s100
	s_lshl_b32 s100, s100, 12
	s_lshl_b32 s99, s99, 9
	v_lshl_add_u32 v244, v130, 6, s100
	v_lshl_add_u32 v249, v130, 2, s99
	v_readlane_b32 s100, v255, 7
	v_readlane_b32 s101, v255, 9
	s_nop 4
	global_load_dwordx4 v[212:215], v244, s[100:101] offset:48
	global_load_dwordx4 v[216:219], v244, s[100:101] offset:32
	global_load_dwordx4 v[220:223], v244, s[100:101] offset:16
	global_load_dwordx4 v[224:227], v244, s[100:101]
	v_readlane_b32 s100, v254, 56
	v_readlane_b32 s101, v255, 5
	s_nop 4
	global_load_dwordx4 v[228:231], v244, s[100:101] offset:48
	global_load_dwordx4 v[232:235], v244, s[100:101] offset:32
	global_load_dwordx4 v[236:239], v244, s[100:101] offset:16
	global_load_dwordx4 v[240:243], v244, s[100:101]
	global_load_dword v245, v249, s[70:71] offset:256
	global_load_dword v246, v249, s[40:41] offset:256
	global_load_dword v247, v249, s[40:41]
	global_load_dword v248, v249, s[70:71]
	v_readlane_b32 s98, v254, 55
	s_cmp_lt_u32 s98, 4
	s_cbranch_scc1 .Lprio_lo
	s_setprio 1
.Lprio_lo:
	s_branch .LBB0_1416
;     ...
;         if (!dummy && !OF) {
;             float am = 0.f;
; #pragma unroll
;             for (int i = 0; i < 16; ++i) am = fmaxf(am, fmaxf(fabsf(acc[i].x), fabsf(acc[i].y)));
;             am = wave_max(am);
;             const float inv = (am > 0.f) ? 127.0f / am : 0.f;
;             if (lane2 == 0) ((float*)(F.ws + WS_SX))[t] = am * (1.0f / 127.0f);
; #pragma unroll
;             for (int hh = 0; hh < 4; ++hh) { v2u y8; y8.x = pk4_i8(acc[hh * 4].x * inv, acc[hh * 4].y * inv, acc[hh * 4 + 1].x * inv, acc[hh * 4 + 1].y * inv);
;                 y8.y = pk4_i8(acc[hh * 4 + 2].x * inv, acc[hh * 4 + 2].y * inv, acc[hh * 4 + 3].x * inv, acc[hh * 4 + 3].y * inv);
;                 *(v2u*)(F.ws + WS_X8 + (size_t)t * D + lane2 * 32 + hh * 8) = y8; }
;         }
.LBB0_1414:
	s_or_b64 exec, exec, s[56:57]
	s_mov_b32 s62, 0x42fe0000
	v_div_scale_f32 v99, s[56:57], v98, v98, s62
	v_rcp_f32_e32 v100, v99
	v_div_scale_f32 v101, vcc, s62, v98, s62
	v_readlane_b32 s56, v255, 29
	v_fma_f32 v102, -v99, v100, 1.0
	v_fmac_f32_e32 v100, v102, v100
	v_mul_f32_e32 v102, v101, v100
	v_fma_f32 v103, -v99, v102, v101
	v_fmac_f32_e32 v102, v103, v100
	v_fma_f32 v99, -v99, v102, v101
	v_div_fmas_f32 v99, v99, v100, v102
	v_div_fixup_f32 v99, v99, v98, s62
	v_cmp_lt_f32_e32 vcc, 0, v98
	s_mov_b32 s62, 0xc0c0500
	s_add_u32 s56, s56, s86
	v_cndmask_b32_e32 v98, 0, v99, vcc
	v_mul_f32_e32 v67, v67, v98
	v_mul_f32_e32 v66, v66, v98
	v_mul_f32_e32 v68, v68, v98
	v_rndne_f32_e32 v67, v67
	v_mul_f32_e32 v69, v69, v98
	v_rndne_f32_e32 v66, v66
	v_cvt_i32_f32_e32 v67, v67
	v_rndne_f32_e32 v68, v68
	v_cvt_i32_f32_e32 v66, v66
	v_cvt_i32_f32_sdwa v68, v68 dst_sel:WORD_1 dst_unused:UNUSED_PAD src0_sel:DWORD
	v_rndne_f32_e32 v69, v69
	v_cvt_i32_f32_sdwa v69, v69 dst_sel:BYTE_3 dst_unused:UNUSED_PAD src0_sel:DWORD
	v_lshlrev_b32_e32 v67, 8, v67
	v_and_b32_e32 v68, 0xff0000, v68
	v_perm_b32 v66, v67, v66, s62
	v_or3_b32 v66, v66, v69, v68
	v_mul_f32_e32 v68, v71, v98
	v_mul_f32_e32 v67, v70, v98
	v_mul_f32_e32 v69, v72, v98
	v_rndne_f32_e32 v68, v68
	v_mul_f32_e32 v70, v73, v98
	v_rndne_f32_e32 v67, v67
	v_cvt_i32_f32_e32 v68, v68
	v_rndne_f32_e32 v69, v69
	v_cvt_i32_f32_e32 v67, v67
	v_cvt_i32_f32_sdwa v69, v69 dst_sel:WORD_1 dst_unused:UNUSED_PAD src0_sel:DWORD
	v_rndne_f32_e32 v70, v70
	v_cvt_i32_f32_sdwa v70, v70 dst_sel:BYTE_3 dst_unused:UNUSED_PAD src0_sel:DWORD
	v_lshlrev_b32_e32 v68, 8, v68
	v_and_b32_e32 v69, 0xff0000, v69
	v_perm_b32 v67, v68, v67, s62
	v_or3_b32 v67, v67, v70, v69
	v_mul_f32_e32 v69, v75, v98
	v_mul_f32_e32 v68, v74, v98
	v_mul_f32_e32 v72, v76, v98
	v_rndne_f32_e32 v69, v69
	v_mul_f32_e32 v73, v77, v98
	v_rndne_f32_e32 v68, v68
	v_cvt_i32_f32_e32 v69, v69
	v_rndne_f32_e32 v72, v72
	v_cvt_i32_f32_e32 v68, v68
	v_cvt_i32_f32_sdwa v72, v72 dst_sel:WORD_1 dst_unused:UNUSED_PAD src0_sel:DWORD
	v_rndne_f32_e32 v73, v73
	v_cvt_i32_f32_sdwa v73, v73 dst_sel:BYTE_3 dst_unused:UNUSED_PAD src0_sel:DWORD
	v_lshlrev_b32_e32 v69, 8, v69
	v_and_b32_e32 v72, 0xff0000, v72
	v_perm_b32 v68, v69, v68, s62
	v_or3_b32 v68, v68, v73, v72
	v_mul_f32_e32 v72, v79, v98
	v_mul_f32_e32 v69, v78, v98
	v_mul_f32_e32 v73, v80, v98
	v_rndne_f32_e32 v72, v72
	v_mul_f32_e32 v74, v81, v98
	v_rndne_f32_e32 v69, v69
	v_cvt_i32_f32_e32 v72, v72
	v_rndne_f32_e32 v73, v73
	v_cvt_i32_f32_e32 v69, v69
	v_cvt_i32_f32_sdwa v73, v73 dst_sel:WORD_1 dst_unused:UNUSED_PAD src0_sel:DWORD
	v_rndne_f32_e32 v74, v74
	v_cvt_i32_f32_sdwa v74, v74 dst_sel:BYTE_3 dst_unused:UNUSED_PAD src0_sel:DWORD
	v_readlane_b32 s57, v255, 31
	v_lshlrev_b32_e32 v72, 8, v72
	s_addc_u32 s57, s57, s87
	v_and_b32_e32 v73, 0xff0000, v73
	v_perm_b32 v69, v72, v69, s62
	v_lshl_add_u64 v[70:71], s[56:57], 0, v[134:135]
	v_or3_b32 v69, v69, v74, v73
	global_store_dwordx4 v[70:71], v[66:69], off
	v_mul_f32_e32 v70, v89, v98
	v_rndne_f32_e32 v70, v70
	v_mul_f32_e32 v67, v83, v98
	v_mul_f32_e32 v66, v82, v98
	v_mul_f32_e32 v68, v84, v98
	v_rndne_f32_e32 v67, v67
	v_mul_f32_e32 v69, v85, v98
	v_rndne_f32_e32 v66, v66
	v_cvt_i32_f32_e32 v67, v67
	v_rndne_f32_e32 v68, v68
	v_cvt_i32_f32_e32 v66, v66
	v_cvt_i32_f32_sdwa v68, v68 dst_sel:WORD_1 dst_unused:UNUSED_PAD src0_sel:DWORD
	v_rndne_f32_e32 v69, v69
	v_cvt_i32_f32_sdwa v69, v69 dst_sel:BYTE_3 dst_unused:UNUSED_PAD src0_sel:DWORD
	v_lshlrev_b32_e32 v67, 8, v67
	v_and_b32_e32 v68, 0xff0000, v68
	v_perm_b32 v66, v67, v66, s62
	v_or3_b32 v66, v66, v69, v68
	v_mul_f32_e32 v68, v87, v98
	v_mul_f32_e32 v67, v86, v98
	v_mul_f32_e32 v69, v88, v98
	v_rndne_f32_e32 v68, v68
	v_rndne_f32_e32 v67, v67
	v_cvt_i32_f32_e32 v68, v68
	v_rndne_f32_e32 v69, v69
	v_cvt_i32_f32_e32 v67, v67
	v_cvt_i32_f32_sdwa v69, v69 dst_sel:WORD_1 dst_unused:UNUSED_PAD src0_sel:DWORD
	v_cvt_i32_f32_sdwa v70, v70 dst_sel:BYTE_3 dst_unused:UNUSED_PAD src0_sel:DWORD
	v_lshlrev_b32_e32 v68, 8, v68
	v_perm_b32 v67, v68, v67, s62
	v_and_b32_e32 v69, 0xff0000, v69
	v_or3_b32 v67, v67, v70, v69
	v_mul_f32_e32 v69, v91, v98
	v_mul_f32_e32 v68, v90, v98
	v_mul_f32_e32 v70, v92, v98
	v_rndne_f32_e32 v69, v69
	v_mul_f32_e32 v71, v93, v98
	v_rndne_f32_e32 v68, v68
	v_cvt_i32_f32_e32 v69, v69
	v_rndne_f32_e32 v70, v70
	v_cvt_i32_f32_e32 v68, v68
	v_cvt_i32_f32_sdwa v70, v70 dst_sel:WORD_1 dst_unused:UNUSED_PAD src0_sel:DWORD
	v_rndne_f32_e32 v71, v71
	v_cvt_i32_f32_sdwa v71, v71 dst_sel:BYTE_3 dst_unused:UNUSED_PAD src0_sel:DWORD
	v_lshlrev_b32_e32 v69, 8, v69
	v_and_b32_e32 v70, 0xff0000, v70
	v_perm_b32 v68, v69, v68, s62
	v_or3_b32 v68, v68, v71, v70
	v_mul_f32_e32 v70, v95, v98
	v_mul_f32_e32 v69, v94, v98
	v_mul_f32_e32 v71, v96, v98
	v_rndne_f32_e32 v70, v70
	v_mul_f32_e32 v74, v97, v98
	v_rndne_f32_e32 v69, v69
	v_cvt_i32_f32_e32 v70, v70
	v_rndne_f32_e32 v71, v71
	v_cvt_i32_f32_e32 v69, v69
	v_cvt_i32_f32_sdwa v71, v71 dst_sel:WORD_1 dst_unused:UNUSED_PAD src0_sel:DWORD
	v_rndne_f32_e32 v74, v74
	s_add_u32 s56, s60, s86
	v_cvt_i32_f32_sdwa v74, v74 dst_sel:BYTE_3 dst_unused:UNUSED_PAD src0_sel:DWORD
	s_addc_u32 s57, s61, s87
	v_lshl_add_u64 v[72:73], s[56:57], 0, v[134:135]
	v_lshlrev_b32_e32 v70, 8, v70
	v_and_b32_e32 v71, 0xff0000, v71
	v_perm_b32 v69, v70, v69, s62
	v_add_co_u32_e32 v70, vcc, 0x53600000, v72
	v_or3_b32 v69, v69, v74, v71
	s_nop 0
	v_addc_co_u32_e32 v71, vcc, 0, v73, vcc
	global_store_dwordx4 v[70:71], v[66:69], off offset:16

; #define PH_REP(k) for (int rep_ = 0; rep_ < (((PROBE_REP_MASK >> (k)) & 1) ? 2 : 1); ++rep_)
; #define PH_SEAM(id) do { if ((id) + 1 < hi) xcd_barrier(bar, F.wave == 0 && fresh_lane() == 0); } while (0)
; __global__ void __launch_bounds__(NTHREADS, 2) mk_fwd(Args args) {
;     ...
;         if (PH_IN(pb + 8)) { PH_REP(8) { ph_gather_ln2(F, layer); } PH_SEAM(pb + 8); }
;     ...
;     }
.LBB0_1451:
	s_setprio 0
	v_readlane_b32 s80, v254, 20
	v_readlane_b32 s88, v254, 28
	v_readlane_b32 s81, v254, 21
	v_readlane_b32 s82, v254, 22
	v_readlane_b32 s83, v254, 23
	v_readlane_b32 s84, v254, 24
	v_readlane_b32 s85, v254, 25
	v_readlane_b32 s86, v254, 26
	v_readlane_b32 s87, v254, 27
	v_readlane_b32 s89, v254, 29
	v_readlane_b32 s91, v254, 30
	s_movk_i32 s48, 0x80
	s_movk_i32 s52, 0x7f
	s_mov_b32 s49, 0x42fe0000
	s_mov_b32 s50, 0x5a600000
	s_mov_b32 s51, 0x1e3ce508
	s_mov_b32 s53, 0x42ee0000
	s_mov_b32 s54, 0x55600000
	s_mov_b64 s[78:79], 0x6b600000
	s_mov_b64 s[56:57], 0x2000
	v_readlane_b32 s43, v254, 62
